# P3 attention unit: S^T with double-buffered K fragments, arithmetic band masks + batched unconditional bias reads instead of 40 exec-masked LDS round trips, in-place softmax, v_rcp for 1/lsum, double-
# speedup vs baseline: 1.0305x; 1.0305x over previous
.LBB0_725:
	s_lshr_b32 s10, 64, s25
	s_and_b32 s42, s42, 63
	s_add_i32 s10, s10, -1
	s_and_b32 s44, s10, s42
	ds_read_b128 v[218:221], v201
	ds_read_b128 v[222:225], v201 offset:64
	ds_read_b128 v[226:229], v201 offset:128
	ds_read_b128 v[230:233], v201 offset:192
	ds_read_b128 v[234:237], v202
	ds_read_b128 v[238:241], v202 offset:64
	ds_read_b128 v[242:245], v202 offset:128
	ds_read_b128 v[246:249], v202 offset:192
	v_lshrrev_b32_e32 v250, 7, v0
	v_bfe_u32 v251, v0, 4, 2
	v_lshlrev_b32_e32 v250, 5, v250
	v_lshl_add_u32 v250, v251, 2, v250
	v_sub_u32_e32 v250, v149, v250
	v_add_u32_e32 v250, 0x80, v250
	s_mov_b32 s36, 0x21d84
	s_cmp_eq_u32 s44, 0
	s_cselect_b64 s[46:47], -1, 0
	v_lshl_add_u32 v251, v250, 2, s36
	v_mov_b32_e32 v252, 0x80
	v_mov_b32_e32 v253, 0xf149f2ca
	v_cndmask_b32_e64 v252, v252, v149, s[46:47]
	s_waitcnt lgkmcnt(7)
	v_mfma_f32_16x16x32_bf16 v[100:103], v[218:221], v[84:87], 0
	s_waitcnt lgkmcnt(6)
	v_mfma_f32_16x16x32_bf16 v[100:103], v[222:225], v[88:91], v[100:103]
	s_waitcnt lgkmcnt(5)
	v_mfma_f32_16x16x32_bf16 v[100:103], v[226:229], v[92:95], v[100:103]
	s_waitcnt lgkmcnt(4)
	v_mfma_f32_16x16x32_bf16 v[100:103], v[230:233], v[96:99], v[100:103]
	ds_read_b128 v[218:221], v203
	ds_read_b128 v[222:225], v203 offset:64
	ds_read_b128 v[226:229], v203 offset:128
	ds_read_b128 v[230:233], v203 offset:192
	s_waitcnt lgkmcnt(7)
	v_mfma_f32_16x16x32_bf16 v[104:107], v[234:237], v[84:87], 0
	s_waitcnt lgkmcnt(6)
	v_mfma_f32_16x16x32_bf16 v[104:107], v[238:241], v[88:91], v[104:107]
	s_waitcnt lgkmcnt(5)
	v_mfma_f32_16x16x32_bf16 v[104:107], v[242:245], v[92:95], v[104:107]
	s_waitcnt lgkmcnt(4)
	v_mfma_f32_16x16x32_bf16 v[104:107], v[246:249], v[96:99], v[104:107]
	ds_read_b128 v[234:237], v204
	ds_read_b128 v[238:241], v204 offset:64
	ds_read_b128 v[242:245], v204 offset:128
	ds_read_b128 v[246:249], v204 offset:192
	s_waitcnt lgkmcnt(7)
	v_mfma_f32_16x16x32_bf16 v[108:111], v[218:221], v[84:87], 0
	s_waitcnt lgkmcnt(6)
	v_mfma_f32_16x16x32_bf16 v[108:111], v[222:225], v[88:91], v[108:111]
	s_waitcnt lgkmcnt(5)
	v_mfma_f32_16x16x32_bf16 v[108:111], v[226:229], v[92:95], v[108:111]
	s_waitcnt lgkmcnt(4)
	v_mfma_f32_16x16x32_bf16 v[108:111], v[230:233], v[96:99], v[108:111]
	ds_read_b128 v[218:221], v205
	ds_read_b128 v[222:225], v205 offset:64
	ds_read_b128 v[226:229], v205 offset:128
	ds_read_b128 v[230:233], v205 offset:192
	s_waitcnt lgkmcnt(7)
	v_mfma_f32_16x16x32_bf16 v[112:115], v[234:237], v[84:87], 0
	s_waitcnt lgkmcnt(6)
	v_mfma_f32_16x16x32_bf16 v[112:115], v[238:241], v[88:91], v[112:115]
	s_waitcnt lgkmcnt(5)
	v_mfma_f32_16x16x32_bf16 v[112:115], v[242:245], v[92:95], v[112:115]
	s_waitcnt lgkmcnt(4)
	v_mfma_f32_16x16x32_bf16 v[112:115], v[246:249], v[96:99], v[112:115]
	ds_read_b128 v[234:237], v206
	ds_read_b128 v[238:241], v206 offset:64
	ds_read_b128 v[242:245], v206 offset:128
	ds_read_b128 v[246:249], v206 offset:192
	s_waitcnt lgkmcnt(7)
	v_mfma_f32_16x16x32_bf16 v[116:119], v[218:221], v[84:87], 0
	s_waitcnt lgkmcnt(6)
	v_mfma_f32_16x16x32_bf16 v[116:119], v[222:225], v[88:91], v[116:119]
	s_waitcnt lgkmcnt(5)
	v_mfma_f32_16x16x32_bf16 v[116:119], v[226:229], v[92:95], v[116:119]
	s_waitcnt lgkmcnt(4)
	v_mfma_f32_16x16x32_bf16 v[116:119], v[230:233], v[96:99], v[116:119]
	ds_read_b128 v[218:221], v207
	ds_read_b128 v[222:225], v207 offset:64
	ds_read_b128 v[226:229], v207 offset:128
	ds_read_b128 v[230:233], v207 offset:192
	s_waitcnt lgkmcnt(7)
	v_mfma_f32_16x16x32_bf16 v[120:123], v[234:237], v[84:87], 0
	s_waitcnt lgkmcnt(6)
	v_mfma_f32_16x16x32_bf16 v[120:123], v[238:241], v[88:91], v[120:123]
	s_waitcnt lgkmcnt(5)
	v_mfma_f32_16x16x32_bf16 v[120:123], v[242:245], v[92:95], v[120:123]
	s_waitcnt lgkmcnt(4)
	v_mfma_f32_16x16x32_bf16 v[120:123], v[246:249], v[96:99], v[120:123]
	ds_read_b128 v[234:237], v208
	ds_read_b128 v[238:241], v208 offset:64
	ds_read_b128 v[242:245], v208 offset:128
	ds_read_b128 v[246:249], v208 offset:192
	s_waitcnt lgkmcnt(7)
	v_mfma_f32_16x16x32_bf16 v[124:127], v[218:221], v[84:87], 0
	s_waitcnt lgkmcnt(6)
	v_mfma_f32_16x16x32_bf16 v[124:127], v[222:225], v[88:91], v[124:127]
	s_waitcnt lgkmcnt(5)
	v_mfma_f32_16x16x32_bf16 v[124:127], v[226:229], v[92:95], v[124:127]
	s_waitcnt lgkmcnt(4)
	v_mfma_f32_16x16x32_bf16 v[124:127], v[230:233], v[96:99], v[124:127]
	ds_read_b128 v[218:221], v209
	ds_read_b128 v[222:225], v209 offset:64
	ds_read_b128 v[226:229], v209 offset:128
	ds_read_b128 v[230:233], v209 offset:192
	s_waitcnt lgkmcnt(7)
	v_mfma_f32_16x16x32_bf16 v[128:131], v[234:237], v[84:87], 0
	s_waitcnt lgkmcnt(6)
	v_mfma_f32_16x16x32_bf16 v[128:131], v[238:241], v[88:91], v[128:131]
	s_waitcnt lgkmcnt(5)
	v_mfma_f32_16x16x32_bf16 v[128:131], v[242:245], v[92:95], v[128:131]
	s_waitcnt lgkmcnt(4)
	v_mfma_f32_16x16x32_bf16 v[128:131], v[246:249], v[96:99], v[128:131]
	ds_read_b128 v[234:237], v210
	ds_read_b128 v[238:241], v210 offset:64
	ds_read_b128 v[242:245], v210 offset:128
	ds_read_b128 v[246:249], v210 offset:192
	s_waitcnt lgkmcnt(7)
	v_mfma_f32_16x16x32_bf16 v[132:135], v[218:221], v[84:87], 0
	s_waitcnt lgkmcnt(6)
	v_mfma_f32_16x16x32_bf16 v[132:135], v[222:225], v[88:91], v[132:135]
	s_waitcnt lgkmcnt(5)
	v_mfma_f32_16x16x32_bf16 v[132:135], v[226:229], v[92:95], v[132:135]
	s_waitcnt lgkmcnt(4)
	v_mfma_f32_16x16x32_bf16 v[132:135], v[230:233], v[96:99], v[132:135]
	s_waitcnt lgkmcnt(3)
	v_mfma_f32_16x16x32_bf16 v[214:217], v[234:237], v[84:87], 0
	s_waitcnt lgkmcnt(2)
	v_mfma_f32_16x16x32_bf16 v[214:217], v[238:241], v[88:91], v[214:217]
	s_waitcnt lgkmcnt(1)
	v_mfma_f32_16x16x32_bf16 v[214:217], v[242:245], v[92:95], v[214:217]
	s_waitcnt lgkmcnt(0)
	v_mfma_f32_16x16x32_bf16 v[214:217], v[246:249], v[96:99], v[214:217]
	ds_read_b32 v218, v251 offset:636
	ds_read_b32 v219, v251 offset:632
	ds_read_b32 v220, v251 offset:628
	ds_read_b32 v221, v251 offset:624
	ds_read_b32 v222, v251 offset:572
	ds_read_b32 v223, v251 offset:568
	ds_read_b32 v224, v251 offset:564
	ds_read_b32 v225, v251 offset:560
	ds_read_b32 v226, v251 offset:508
	ds_read_b32 v227, v251 offset:504
	ds_read_b32 v228, v251 offset:500
	ds_read_b32 v229, v251 offset:496
	ds_read_b32 v230, v251 offset:444
	ds_read_b32 v231, v251 offset:440
	ds_read_b32 v232, v251 offset:436
	ds_read_b32 v233, v251 offset:432
	ds_read_b32 v234, v251 offset:380
	ds_read_b32 v235, v251 offset:376
	ds_read_b32 v236, v251 offset:372
	ds_read_b32 v237, v251 offset:368
	ds_read_b32 v238, v251 offset:316
	ds_read_b32 v239, v251 offset:312
	ds_read_b32 v240, v251 offset:308
	ds_read_b32 v241, v251 offset:304
	s_nop 3
	s_waitcnt lgkmcnt(12)
	v_subrev_u32_e32 v242, 0, v250
	v_subrev_u32_e32 v243, 1, v250
	v_subrev_u32_e32 v244, 2, v250
	v_subrev_u32_e32 v245, 3, v250
	v_cmp_ge_u32_e64 s[98:99], v252, v242
	v_cmp_ge_u32_e64 s[100:101], v252, v243
	v_cmp_ge_u32_e64 s[36:37], v252, v244
	v_cmp_ge_u32_e64 s[46:47], v252, v245
	v_add_f32_e32 v218, v100, v218
	v_add_f32_e32 v219, v101, v219
	v_add_f32_e32 v220, v102, v220
	v_add_f32_e32 v221, v103, v221
	v_cndmask_b32_e64 v100, v253, v218, s[98:99]
	v_cndmask_b32_e64 v101, v253, v219, s[100:101]
	v_cndmask_b32_e64 v102, v253, v220, s[36:37]
	v_cndmask_b32_e64 v103, v253, v221, s[46:47]
	v_subrev_u32_e32 v242, 16, v250
	v_subrev_u32_e32 v243, 17, v250
	v_subrev_u32_e32 v244, 18, v250
	v_subrev_u32_e32 v245, 19, v250
	v_cmp_ge_u32_e64 s[98:99], v252, v242
	v_cmp_ge_u32_e64 s[100:101], v252, v243
	v_cmp_ge_u32_e64 s[36:37], v252, v244
	v_cmp_ge_u32_e64 s[46:47], v252, v245
	v_add_f32_e32 v222, v104, v222
	v_add_f32_e32 v223, v105, v223
	v_add_f32_e32 v224, v106, v224
	v_add_f32_e32 v225, v107, v225
	v_cndmask_b32_e64 v104, v253, v222, s[98:99]
	v_cndmask_b32_e64 v105, v253, v223, s[100:101]
	v_cndmask_b32_e64 v106, v253, v224, s[36:37]
	v_cndmask_b32_e64 v107, v253, v225, s[46:47]
	v_subrev_u32_e32 v242, 32, v250
	v_subrev_u32_e32 v243, 33, v250
	v_subrev_u32_e32 v244, 34, v250
	v_subrev_u32_e32 v245, 35, v250
	v_cmp_ge_u32_e64 s[98:99], v252, v242
	v_cmp_ge_u32_e64 s[100:101], v252, v243
	v_cmp_ge_u32_e64 s[36:37], v252, v244
	v_cmp_ge_u32_e64 s[46:47], v252, v245
	v_add_f32_e32 v226, v108, v226
	v_add_f32_e32 v227, v109, v227
	v_add_f32_e32 v228, v110, v228
	v_add_f32_e32 v229, v111, v229
	v_cndmask_b32_e64 v108, v253, v226, s[98:99]
	v_cndmask_b32_e64 v109, v253, v227, s[100:101]
	v_cndmask_b32_e64 v110, v253, v228, s[36:37]
	v_cndmask_b32_e64 v111, v253, v229, s[46:47]
	ds_read_b32 v218, v251 offset:252
	ds_read_b32 v219, v251 offset:248
	ds_read_b32 v220, v251 offset:244
	ds_read_b32 v221, v251 offset:240
	ds_read_b32 v222, v251 offset:188
	ds_read_b32 v223, v251 offset:184
	ds_read_b32 v224, v251 offset:180
	ds_read_b32 v225, v251 offset:176
	ds_read_b32 v226, v251 offset:124
	ds_read_b32 v227, v251 offset:120
	ds_read_b32 v228, v251 offset:116
	ds_read_b32 v229, v251 offset:112
	s_waitcnt lgkmcnt(12)
	v_subrev_u32_e32 v242, 48, v250
	v_subrev_u32_e32 v243, 49, v250
	v_subrev_u32_e32 v244, 50, v250
	v_subrev_u32_e32 v245, 51, v250
	v_cmp_ge_u32_e64 s[98:99], v252, v242
	v_cmp_ge_u32_e64 s[100:101], v252, v243
	v_cmp_ge_u32_e64 s[36:37], v252, v244
	v_cmp_ge_u32_e64 s[46:47], v252, v245
	v_add_f32_e32 v230, v112, v230
	v_add_f32_e32 v231, v113, v231
	v_add_f32_e32 v232, v114, v232
	v_add_f32_e32 v233, v115, v233
	v_cndmask_b32_e64 v112, v253, v230, s[98:99]
	v_cndmask_b32_e64 v113, v253, v231, s[100:101]
	v_cndmask_b32_e64 v114, v253, v232, s[36:37]
	v_cndmask_b32_e64 v115, v253, v233, s[46:47]
	v_subrev_u32_e32 v242, 64, v250
	v_subrev_u32_e32 v243, 65, v250
	v_subrev_u32_e32 v244, 66, v250
	v_subrev_u32_e32 v245, 67, v250
	v_cmp_ge_u32_e64 s[98:99], v252, v242
	v_cmp_ge_u32_e64 s[100:101], v252, v243
	v_cmp_ge_u32_e64 s[36:37], v252, v244
	v_cmp_ge_u32_e64 s[46:47], v252, v245
	v_add_f32_e32 v234, v116, v234
	v_add_f32_e32 v235, v117, v235
	v_add_f32_e32 v236, v118, v236
	v_add_f32_e32 v237, v119, v237
	v_cndmask_b32_e64 v116, v253, v234, s[98:99]
	v_cndmask_b32_e64 v117, v253, v235, s[100:101]
	v_cndmask_b32_e64 v118, v253, v236, s[36:37]
	v_cndmask_b32_e64 v119, v253, v237, s[46:47]
	v_subrev_u32_e32 v242, 80, v250
	v_subrev_u32_e32 v243, 81, v250
	v_subrev_u32_e32 v244, 82, v250
	v_subrev_u32_e32 v245, 83, v250
	v_cmp_ge_u32_e64 s[98:99], v252, v242
	v_cmp_ge_u32_e64 s[100:101], v252, v243
	v_cmp_ge_u32_e64 s[36:37], v252, v244
	v_cmp_ge_u32_e64 s[46:47], v252, v245
	v_add_f32_e32 v238, v120, v238
	v_add_f32_e32 v239, v121, v239
	v_add_f32_e32 v240, v122, v240
	v_add_f32_e32 v241, v123, v241
	v_cndmask_b32_e64 v120, v253, v238, s[98:99]
	v_cndmask_b32_e64 v121, v253, v239, s[100:101]
	v_cndmask_b32_e64 v122, v253, v240, s[36:37]
	v_cndmask_b32_e64 v123, v253, v241, s[46:47]
	ds_read_b32 v230, v251 offset:60
	ds_read_b32 v231, v251 offset:56
	ds_read_b32 v232, v251 offset:52
	ds_read_b32 v233, v251 offset:48
	s_waitcnt lgkmcnt(4)
	v_subrev_u32_e32 v242, 96, v250
	v_subrev_u32_e32 v243, 97, v250
	v_subrev_u32_e32 v244, 98, v250
	v_subrev_u32_e32 v245, 99, v250
	v_cmp_ge_u32_e64 s[98:99], v252, v242
	v_cmp_ge_u32_e64 s[100:101], v252, v243
	v_cmp_ge_u32_e64 s[36:37], v252, v244
	v_cmp_ge_u32_e64 s[46:47], v252, v245
	v_add_f32_e32 v218, v124, v218
	v_add_f32_e32 v219, v125, v219
	v_add_f32_e32 v220, v126, v220
	v_add_f32_e32 v221, v127, v221
	v_cndmask_b32_e64 v124, v253, v218, s[98:99]
	v_cndmask_b32_e64 v125, v253, v219, s[100:101]
	v_cndmask_b32_e64 v126, v253, v220, s[36:37]
	v_cndmask_b32_e64 v127, v253, v221, s[46:47]
	v_subrev_u32_e32 v242, 112, v250
	v_subrev_u32_e32 v243, 113, v250
	v_subrev_u32_e32 v244, 114, v250
	v_subrev_u32_e32 v245, 115, v250
	v_cmp_ge_u32_e64 s[98:99], v252, v242
	v_cmp_ge_u32_e64 s[100:101], v252, v243
	v_cmp_ge_u32_e64 s[36:37], v252, v244
	v_cmp_ge_u32_e64 s[46:47], v252, v245
	v_add_f32_e32 v222, v128, v222
	v_add_f32_e32 v223, v129, v223
	v_add_f32_e32 v224, v130, v224
	v_add_f32_e32 v225, v131, v225
	v_cndmask_b32_e64 v128, v253, v222, s[98:99]
	v_cndmask_b32_e64 v129, v253, v223, s[100:101]
	v_cndmask_b32_e64 v130, v253, v224, s[36:37]
	v_cndmask_b32_e64 v131, v253, v225, s[46:47]
	v_subrev_u32_e32 v242, 128, v250
	v_subrev_u32_e32 v243, 129, v250
	v_subrev_u32_e32 v244, 130, v250
	v_subrev_u32_e32 v245, 131, v250
	v_cmp_ge_u32_e64 s[98:99], v252, v242
	v_cmp_ge_u32_e64 s[100:101], v252, v243
	v_cmp_ge_u32_e64 s[36:37], v252, v244
	v_cmp_ge_u32_e64 s[46:47], v252, v245
	v_add_f32_e32 v226, v132, v226
	v_add_f32_e32 v227, v133, v227
	v_add_f32_e32 v228, v134, v228
	v_add_f32_e32 v229, v135, v229
	v_cndmask_b32_e64 v132, v253, v226, s[98:99]
	v_cndmask_b32_e64 v133, v253, v227, s[100:101]
	v_cndmask_b32_e64 v134, v253, v228, s[36:37]
	v_cndmask_b32_e64 v135, v253, v229, s[46:47]
	s_waitcnt lgkmcnt(0)
	v_subrev_u32_e32 v242, 144, v250
	v_subrev_u32_e32 v243, 145, v250
	v_subrev_u32_e32 v244, 146, v250
	v_subrev_u32_e32 v245, 147, v250
	v_cmp_ge_u32_e64 s[98:99], v252, v242
	v_cmp_ge_u32_e64 s[100:101], v252, v243
	v_cmp_ge_u32_e64 s[36:37], v252, v244
	v_cmp_ge_u32_e64 s[46:47], v252, v245
	v_add_f32_e32 v230, v214, v230
	v_add_f32_e32 v231, v215, v231
	v_add_f32_e32 v232, v216, v232
	v_add_f32_e32 v233, v217, v233
	v_cndmask_b32_e64 v214, v253, v230, s[98:99]
	v_cndmask_b32_e64 v215, v253, v231, s[100:101]
	v_cndmask_b32_e64 v216, v253, v232, s[36:37]
	v_cndmask_b32_e64 v217, v253, v233, s[46:47]
	v_max3_f32 v242, v100, v101, v102
	v_max3_f32 v243, v120, v121, v122
	v_max3_f32 v242, v242, v103, v104
	v_max3_f32 v243, v243, v123, v124
	v_max3_f32 v242, v242, v105, v106
	v_max3_f32 v243, v243, v125, v126
	v_max3_f32 v242, v242, v107, v108
	v_max3_f32 v243, v243, v127, v128
	v_max3_f32 v242, v242, v109, v110
	v_max3_f32 v243, v243, v129, v130
	v_max3_f32 v242, v242, v111, v112
	v_max3_f32 v243, v243, v131, v132
	v_max3_f32 v242, v242, v113, v114
	v_max3_f32 v243, v243, v133, v134
	v_max3_f32 v242, v242, v115, v116
	v_max3_f32 v243, v243, v135, v214
	v_max3_f32 v242, v242, v117, v118
	v_max3_f32 v243, v243, v215, v216
	v_max_f32_e32 v242, v242, v119
	v_max_f32_e32 v243, v243, v217
	v_max_f32_e32 v47, v242, v243
	s_nop 0
	ds_bpermute_b32 v242, v153, v47
	s_waitcnt lgkmcnt(0)
	v_max_f32_e32 v47, v47, v242
	s_nop 0
	ds_bpermute_b32 v242, v154, v47
	s_waitcnt lgkmcnt(0)
	v_max_f32_e32 v47, v47, v242
	v_sub_f32_e32 v100, v100, v47
	v_sub_f32_e32 v101, v101, v47
	v_sub_f32_e32 v102, v102, v47
	v_sub_f32_e32 v103, v103, v47
	v_mul_f32_e32 v100, 0x3fb8aa3b, v100
	v_mul_f32_e32 v101, 0x3fb8aa3b, v101
	v_mul_f32_e32 v102, 0x3fb8aa3b, v102
	v_mul_f32_e32 v103, 0x3fb8aa3b, v103
	v_exp_f32_e32 v100, v100
	v_exp_f32_e32 v101, v101
	v_exp_f32_e32 v102, v102
	v_exp_f32_e32 v103, v103
	v_sub_f32_e32 v104, v104, v47
	v_sub_f32_e32 v105, v105, v47
	v_sub_f32_e32 v106, v106, v47
	v_sub_f32_e32 v107, v107, v47
	v_mul_f32_e32 v104, 0x3fb8aa3b, v104
	v_mul_f32_e32 v105, 0x3fb8aa3b, v105
	v_mul_f32_e32 v106, 0x3fb8aa3b, v106
	v_mul_f32_e32 v107, 0x3fb8aa3b, v107
	v_exp_f32_e32 v104, v104
	v_exp_f32_e32 v105, v105
	v_exp_f32_e32 v106, v106
	v_exp_f32_e32 v107, v107
	v_add_f32_e32 v238, v100, v104
	v_add_f32_e32 v239, v101, v105
	v_add_f32_e32 v240, v102, v106
	v_add_f32_e32 v241, v103, v107
	v_sub_f32_e32 v108, v108, v47
	v_sub_f32_e32 v109, v109, v47
	v_sub_f32_e32 v110, v110, v47
	v_sub_f32_e32 v111, v111, v47
	v_mul_f32_e32 v108, 0x3fb8aa3b, v108
	v_mul_f32_e32 v109, 0x3fb8aa3b, v109
	v_mul_f32_e32 v110, 0x3fb8aa3b, v110
	v_mul_f32_e32 v111, 0x3fb8aa3b, v111
	v_exp_f32_e32 v108, v108
	v_exp_f32_e32 v109, v109
	v_exp_f32_e32 v110, v110
	v_exp_f32_e32 v111, v111
	v_add_f32_e32 v238, v238, v104
	v_add_f32_e32 v239, v239, v105
	v_add_f32_e32 v240, v240, v106
	v_add_f32_e32 v241, v241, v107
	v_sub_f32_e32 v112, v112, v47
	v_sub_f32_e32 v113, v113, v47
	v_sub_f32_e32 v114, v114, v47
	v_sub_f32_e32 v115, v115, v47
	v_mul_f32_e32 v112, 0x3fb8aa3b, v112
	v_mul_f32_e32 v113, 0x3fb8aa3b, v113
	v_mul_f32_e32 v114, 0x3fb8aa3b, v114
	v_mul_f32_e32 v115, 0x3fb8aa3b, v115
	v_exp_f32_e32 v112, v112
	v_exp_f32_e32 v113, v113
	v_exp_f32_e32 v114, v114
	v_exp_f32_e32 v115, v115
	v_add_f32_e32 v238, v238, v108
	v_add_f32_e32 v239, v239, v109
	v_add_f32_e32 v240, v240, v110
	v_add_f32_e32 v241, v241, v111
	v_sub_f32_e32 v116, v116, v47
	v_sub_f32_e32 v117, v117, v47
	v_sub_f32_e32 v118, v118, v47
	v_sub_f32_e32 v119, v119, v47
	v_mul_f32_e32 v116, 0x3fb8aa3b, v116
	v_mul_f32_e32 v117, 0x3fb8aa3b, v117
	v_mul_f32_e32 v118, 0x3fb8aa3b, v118
	v_mul_f32_e32 v119, 0x3fb8aa3b, v119
	v_exp_f32_e32 v116, v116
	v_exp_f32_e32 v117, v117
	v_exp_f32_e32 v118, v118
	v_exp_f32_e32 v119, v119
	v_add_f32_e32 v238, v238, v112
	v_add_f32_e32 v239, v239, v113
	v_add_f32_e32 v240, v240, v114
	v_add_f32_e32 v241, v241, v115
	v_sub_f32_e32 v120, v120, v47
	v_sub_f32_e32 v121, v121, v47
	v_sub_f32_e32 v122, v122, v47
	v_sub_f32_e32 v123, v123, v47
	v_mul_f32_e32 v120, 0x3fb8aa3b, v120
	v_mul_f32_e32 v121, 0x3fb8aa3b, v121
	v_mul_f32_e32 v122, 0x3fb8aa3b, v122
	v_mul_f32_e32 v123, 0x3fb8aa3b, v123
	v_exp_f32_e32 v120, v120
	v_exp_f32_e32 v121, v121
	v_exp_f32_e32 v122, v122
	v_exp_f32_e32 v123, v123
	v_add_f32_e32 v238, v238, v116
	v_add_f32_e32 v239, v239, v117
	v_add_f32_e32 v240, v240, v118
	v_add_f32_e32 v241, v241, v119
	v_sub_f32_e32 v124, v124, v47
	v_sub_f32_e32 v125, v125, v47
	v_sub_f32_e32 v126, v126, v47
	v_sub_f32_e32 v127, v127, v47
	v_mul_f32_e32 v124, 0x3fb8aa3b, v124
	v_mul_f32_e32 v125, 0x3fb8aa3b, v125
	v_mul_f32_e32 v126, 0x3fb8aa3b, v126
	v_mul_f32_e32 v127, 0x3fb8aa3b, v127
	v_exp_f32_e32 v124, v124
	v_exp_f32_e32 v125, v125
	v_exp_f32_e32 v126, v126
	v_exp_f32_e32 v127, v127
	v_add_f32_e32 v238, v238, v120
	v_add_f32_e32 v239, v239, v121
	v_add_f32_e32 v240, v240, v122
	v_add_f32_e32 v241, v241, v123
	v_sub_f32_e32 v128, v128, v47
	v_sub_f32_e32 v129, v129, v47
	v_sub_f32_e32 v130, v130, v47
	v_sub_f32_e32 v131, v131, v47
	v_mul_f32_e32 v128, 0x3fb8aa3b, v128
	v_mul_f32_e32 v129, 0x3fb8aa3b, v129
	v_mul_f32_e32 v130, 0x3fb8aa3b, v130
	v_mul_f32_e32 v131, 0x3fb8aa3b, v131
	v_exp_f32_e32 v128, v128
	v_exp_f32_e32 v129, v129
	v_exp_f32_e32 v130, v130
	v_exp_f32_e32 v131, v131
	v_add_f32_e32 v238, v238, v124
	v_add_f32_e32 v239, v239, v125
	v_add_f32_e32 v240, v240, v126
	v_add_f32_e32 v241, v241, v127
	v_sub_f32_e32 v132, v132, v47
	v_sub_f32_e32 v133, v133, v47
	v_sub_f32_e32 v134, v134, v47
	v_sub_f32_e32 v135, v135, v47
	v_mul_f32_e32 v132, 0x3fb8aa3b, v132
	v_mul_f32_e32 v133, 0x3fb8aa3b, v133
	v_mul_f32_e32 v134, 0x3fb8aa3b, v134
	v_mul_f32_e32 v135, 0x3fb8aa3b, v135
	v_exp_f32_e32 v132, v132
	v_exp_f32_e32 v133, v133
	v_exp_f32_e32 v134, v134
	v_exp_f32_e32 v135, v135
	v_add_f32_e32 v238, v238, v128
	v_add_f32_e32 v239, v239, v129
	v_add_f32_e32 v240, v240, v130
	v_add_f32_e32 v241, v241, v131
	v_sub_f32_e32 v214, v214, v47
	v_sub_f32_e32 v215, v215, v47
	v_sub_f32_e32 v216, v216, v47
	v_sub_f32_e32 v217, v217, v47
	v_mul_f32_e32 v214, 0x3fb8aa3b, v214
	v_mul_f32_e32 v215, 0x3fb8aa3b, v215
	v_mul_f32_e32 v216, 0x3fb8aa3b, v216
	v_mul_f32_e32 v217, 0x3fb8aa3b, v217
	v_exp_f32_e32 v214, v214
	v_exp_f32_e32 v215, v215
	v_exp_f32_e32 v216, v216
	v_exp_f32_e32 v217, v217
	v_add_f32_e32 v238, v238, v132
	v_add_f32_e32 v239, v239, v133
	v_add_f32_e32 v240, v240, v134
	v_add_f32_e32 v241, v241, v135
	v_add_f32_e32 v238, v238, v214
	v_add_f32_e32 v239, v239, v215
	v_add_f32_e32 v240, v240, v216
	v_add_f32_e32 v241, v241, v217
	v_add_f32_e32 v238, v238, v239
	v_add_f32_e32 v240, v240, v241
	v_add_f32_e32 v238, v238, v240
	ds_bpermute_b32 v239, v153, v238
	v_cvt_pk_bf16_f32 v84, v100, v101
	v_cvt_pk_bf16_f32 v85, v102, v103
	v_cvt_pk_bf16_f32 v86, v104, v105
	v_cvt_pk_bf16_f32 v87, v106, v107
	v_cvt_pk_bf16_f32 v88, v108, v109
	v_cvt_pk_bf16_f32 v89, v110, v111
	v_cvt_pk_bf16_f32 v90, v112, v113
	v_cvt_pk_bf16_f32 v91, v114, v115
	v_cvt_pk_bf16_f32 v92, v116, v117
	v_cvt_pk_bf16_f32 v93, v118, v119
	v_cvt_pk_bf16_f32 v94, v120, v121
	v_cvt_pk_bf16_f32 v95, v122, v123
	v_cvt_pk_bf16_f32 v96, v124, v125
	v_cvt_pk_bf16_f32 v97, v126, v127
	v_cvt_pk_bf16_f32 v98, v128, v129
	v_cvt_pk_bf16_f32 v99, v130, v131
	v_cvt_pk_bf16_f32 v100, v132, v133
	v_cvt_pk_bf16_f32 v101, v134, v135
	v_cvt_pk_bf16_f32 v102, v214, v215
	v_cvt_pk_bf16_f32 v103, v216, v217
	s_waitcnt lgkmcnt(0)
	v_add_f32_e32 v238, v238, v239
	s_nop 0
	ds_bpermute_b32 v239, v154, v238
	ds_read_b64_tr_b16 v[218:219], v150
	ds_read_b64_tr_b16 v[220:221], v150 offset:4352
	ds_read_b64_tr_b16 v[222:223], v150 offset:8704
	ds_read_b64_tr_b16 v[224:225], v150 offset:13056
	ds_read_b64_tr_b16 v[226:227], v150 offset:17408
	ds_read_b64_tr_b16 v[228:229], v150 offset:21760
	ds_read_b64_tr_b16 v[230:231], v150 offset:26112
	ds_read_b64_tr_b16 v[232:233], v150 offset:30464
	ds_read_b64_tr_b16 v[234:235], v150 offset:34816
	ds_read_b64_tr_b16 v[236:237], v150 offset:39168
	v_lshl_add_u32 v242, s44, 7, v149
	v_lshlrev_b32_e32 v242, s25, v242
	s_sub_i32 s10, 6, s25
	s_lshr_b32 s25, s42, s10
	s_lshl_b32 s10, s20, 13
	s_or_b32 s10, s25, s10
	v_add_u32_e32 v107, s10, v242
	v_lshlrev_b32_e32 v104, 10, v107
	v_mov_b32_e32 v105, v46
	v_lshl_add_u64 v[104:105], s[30:31], 0, v[104:105]
	s_lshl_b32 s20, s24, 7
	v_lshl_add_u64 v[104:105], v[104:105], 0, s[20:21]
	v_lshl_add_u64 v[104:105], v[104:105], 0, v[136:137]
	s_waitcnt lgkmcnt(10)
	v_add_f32_e32 v106, v238, v239
	s_nop 0
	v_rcp_f32_e32 v250, v106
	s_nop 0
	v_mul_f32_e32 v250, 0x42000000, v250
	ds_read_b64_tr_b16 v[108:109], v150 offset:32
	ds_read_b64_tr_b16 v[110:111], v150 offset:4384
	ds_read_b64_tr_b16 v[112:113], v150 offset:8736
	ds_read_b64_tr_b16 v[114:115], v150 offset:13088
	ds_read_b64_tr_b16 v[116:117], v150 offset:17440
	s_waitcnt lgkmcnt(13)
	v_mfma_f32_16x16x32_bf16 v[128:131], v[218:221], v[84:87], 0
	s_waitcnt lgkmcnt(11)
	v_mfma_f32_16x16x32_bf16 v[128:131], v[222:225], v[88:91], v[128:131]
	s_waitcnt lgkmcnt(9)
	v_mfma_f32_16x16x32_bf16 v[128:131], v[226:229], v[92:95], v[128:131]
	s_waitcnt lgkmcnt(7)
	v_mfma_f32_16x16x32_bf16 v[128:131], v[230:233], v[96:99], v[128:131]
	s_waitcnt lgkmcnt(5)
	v_mfma_f32_16x16x32_bf16 v[128:131], v[234:237], v[100:103], v[128:131]
	ds_read_b64_tr_b16 v[118:119], v150 offset:21792
	ds_read_b64_tr_b16 v[120:121], v150 offset:26144
	ds_read_b64_tr_b16 v[122:123], v150 offset:30496
	ds_read_b64_tr_b16 v[124:125], v150 offset:34848
	ds_read_b64_tr_b16 v[126:127], v150 offset:39200
	s_nop 2
	v_mul_f32_e32 v128, v250, v128
	v_mul_f32_e32 v129, v250, v129
	v_mul_f32_e32 v130, v250, v130
	v_mul_f32_e32 v131, v250, v131
	v_med3_f32 v128, v128, s41, v212
	v_med3_f32 v129, v129, s41, v212
	v_med3_f32 v130, v130, s41, v212
	v_med3_f32 v131, v131, s41, v212
	v_cvt_pk_fp8_f32 v251, v128, v129
	s_nop 0
	v_cvt_pk_fp8_f32 v251, v130, v131 op_sel:[0,0,1]
	s_nop 0
	global_store_dword v[104:105], v251, off
	ds_read_b64_tr_b16 v[218:219], v150 offset:64
	ds_read_b64_tr_b16 v[220:221], v150 offset:4416
	ds_read_b64_tr_b16 v[222:223], v150 offset:8768
	ds_read_b64_tr_b16 v[224:225], v150 offset:13120
	ds_read_b64_tr_b16 v[226:227], v150 offset:17472
	s_waitcnt lgkmcnt(13)
	v_mfma_f32_16x16x32_bf16 v[132:135], v[108:111], v[84:87], 0
	s_waitcnt lgkmcnt(11)
	v_mfma_f32_16x16x32_bf16 v[132:135], v[112:115], v[88:91], v[132:135]
	s_waitcnt lgkmcnt(9)
	v_mfma_f32_16x16x32_bf16 v[132:135], v[116:119], v[92:95], v[132:135]
	s_waitcnt lgkmcnt(7)
	v_mfma_f32_16x16x32_bf16 v[132:135], v[120:123], v[96:99], v[132:135]
	s_waitcnt lgkmcnt(5)
	v_mfma_f32_16x16x32_bf16 v[132:135], v[124:127], v[100:103], v[132:135]
	ds_read_b64_tr_b16 v[228:229], v150 offset:21824
	ds_read_b64_tr_b16 v[230:231], v150 offset:26176
	ds_read_b64_tr_b16 v[232:233], v150 offset:30528
	ds_read_b64_tr_b16 v[234:235], v150 offset:34880
	ds_read_b64_tr_b16 v[236:237], v150 offset:39232
	s_nop 2
	v_mul_f32_e32 v132, v250, v132
	v_mul_f32_e32 v133, v250, v133
	v_mul_f32_e32 v134, v250, v134
	v_mul_f32_e32 v135, v250, v135
	v_med3_f32 v132, v132, s41, v212
	v_med3_f32 v133, v133, s41, v212
	v_med3_f32 v134, v134, s41, v212
	v_med3_f32 v135, v135, s41, v212
	v_cvt_pk_fp8_f32 v251, v132, v133
	s_nop 0
	v_cvt_pk_fp8_f32 v251, v134, v135 op_sel:[0,0,1]
	s_nop 0
	global_store_dword v[104:105], v251, off offset:16
	ds_read_b64_tr_b16 v[108:109], v150 offset:96
	ds_read_b64_tr_b16 v[110:111], v150 offset:4448
	ds_read_b64_tr_b16 v[112:113], v150 offset:8800
	ds_read_b64_tr_b16 v[114:115], v150 offset:13152
	ds_read_b64_tr_b16 v[116:117], v150 offset:17504
	s_waitcnt lgkmcnt(13)
	v_mfma_f32_16x16x32_bf16 v[128:131], v[218:221], v[84:87], 0
	s_waitcnt lgkmcnt(11)
	v_mfma_f32_16x16x32_bf16 v[128:131], v[222:225], v[88:91], v[128:131]
	s_waitcnt lgkmcnt(9)
	v_mfma_f32_16x16x32_bf16 v[128:131], v[226:229], v[92:95], v[128:131]
	s_waitcnt lgkmcnt(7)
	v_mfma_f32_16x16x32_bf16 v[128:131], v[230:233], v[96:99], v[128:131]
	s_waitcnt lgkmcnt(5)
	v_mfma_f32_16x16x32_bf16 v[128:131], v[234:237], v[100:103], v[128:131]
	ds_read_b64_tr_b16 v[118:119], v150 offset:21856
	ds_read_b64_tr_b16 v[120:121], v150 offset:26208
	ds_read_b64_tr_b16 v[122:123], v150 offset:30560
	ds_read_b64_tr_b16 v[124:125], v150 offset:34912
	ds_read_b64_tr_b16 v[126:127], v150 offset:39264
	s_nop 2
	v_mul_f32_e32 v128, v250, v128
	v_mul_f32_e32 v129, v250, v129
	v_mul_f32_e32 v130, v250, v130
	v_mul_f32_e32 v131, v250, v131
	v_med3_f32 v128, v128, s41, v212
	v_med3_f32 v129, v129, s41, v212
	v_med3_f32 v130, v130, s41, v212
	v_med3_f32 v131, v131, s41, v212
	v_cvt_pk_fp8_f32 v251, v128, v129
	s_nop 0
	v_cvt_pk_fp8_f32 v251, v130, v131 op_sel:[0,0,1]
	s_nop 0
	global_store_dword v[104:105], v251, off offset:32
	ds_read_b64_tr_b16 v[218:219], v150 offset:128
	ds_read_b64_tr_b16 v[220:221], v150 offset:4480
	ds_read_b64_tr_b16 v[222:223], v150 offset:8832
	ds_read_b64_tr_b16 v[224:225], v150 offset:13184
	ds_read_b64_tr_b16 v[226:227], v150 offset:17536
	s_waitcnt lgkmcnt(13)
	v_mfma_f32_16x16x32_bf16 v[132:135], v[108:111], v[84:87], 0
	s_waitcnt lgkmcnt(11)
	v_mfma_f32_16x16x32_bf16 v[132:135], v[112:115], v[88:91], v[132:135]
	s_waitcnt lgkmcnt(9)
	v_mfma_f32_16x16x32_bf16 v[132:135], v[116:119], v[92:95], v[132:135]
	s_waitcnt lgkmcnt(7)
	v_mfma_f32_16x16x32_bf16 v[132:135], v[120:123], v[96:99], v[132:135]
	s_waitcnt lgkmcnt(5)
	v_mfma_f32_16x16x32_bf16 v[132:135], v[124:127], v[100:103], v[132:135]
	ds_read_b64_tr_b16 v[228:229], v150 offset:21888
	ds_read_b64_tr_b16 v[230:231], v150 offset:26240
	ds_read_b64_tr_b16 v[232:233], v150 offset:30592
	ds_read_b64_tr_b16 v[234:235], v150 offset:34944
	ds_read_b64_tr_b16 v[236:237], v150 offset:39296
	s_nop 2
	v_mul_f32_e32 v132, v250, v132
	v_mul_f32_e32 v133, v250, v133
	v_mul_f32_e32 v134, v250, v134
	v_mul_f32_e32 v135, v250, v135
	v_med3_f32 v132, v132, s41, v212
	v_med3_f32 v133, v133, s41, v212
	v_med3_f32 v134, v134, s41, v212
	v_med3_f32 v135, v135, s41, v212
	v_cvt_pk_fp8_f32 v251, v132, v133
	s_nop 0
	v_cvt_pk_fp8_f32 v251, v134, v135 op_sel:[0,0,1]
	s_nop 0
	global_store_dword v[104:105], v251, off offset:48
	ds_read_b64_tr_b16 v[108:109], v150 offset:160
	ds_read_b64_tr_b16 v[110:111], v150 offset:4512
	ds_read_b64_tr_b16 v[112:113], v150 offset:8864
	ds_read_b64_tr_b16 v[114:115], v150 offset:13216
	ds_read_b64_tr_b16 v[116:117], v150 offset:17568
	s_waitcnt lgkmcnt(13)
	v_mfma_f32_16x16x32_bf16 v[128:131], v[218:221], v[84:87], 0
	s_waitcnt lgkmcnt(11)
	v_mfma_f32_16x16x32_bf16 v[128:131], v[222:225], v[88:91], v[128:131]
	s_waitcnt lgkmcnt(9)
	v_mfma_f32_16x16x32_bf16 v[128:131], v[226:229], v[92:95], v[128:131]
	s_waitcnt lgkmcnt(7)
	v_mfma_f32_16x16x32_bf16 v[128:131], v[230:233], v[96:99], v[128:131]
	s_waitcnt lgkmcnt(5)
	v_mfma_f32_16x16x32_bf16 v[128:131], v[234:237], v[100:103], v[128:131]
	ds_read_b64_tr_b16 v[118:119], v150 offset:21920
	ds_read_b64_tr_b16 v[120:121], v150 offset:26272
	ds_read_b64_tr_b16 v[122:123], v150 offset:30624
	ds_read_b64_tr_b16 v[124:125], v150 offset:34976
	ds_read_b64_tr_b16 v[126:127], v150 offset:39328
	s_nop 2
	v_mul_f32_e32 v128, v250, v128
	v_mul_f32_e32 v129, v250, v129
	v_mul_f32_e32 v130, v250, v130
	v_mul_f32_e32 v131, v250, v131
	v_med3_f32 v128, v128, s41, v212
	v_med3_f32 v129, v129, s41, v212
	v_med3_f32 v130, v130, s41, v212
	v_med3_f32 v131, v131, s41, v212
	v_cvt_pk_fp8_f32 v251, v128, v129
	s_nop 0
	v_cvt_pk_fp8_f32 v251, v130, v131 op_sel:[0,0,1]
	s_nop 0
	global_store_dword v[104:105], v251, off offset:64
	ds_read_b64_tr_b16 v[218:219], v150 offset:192
	ds_read_b64_tr_b16 v[220:221], v150 offset:4544
	ds_read_b64_tr_b16 v[222:223], v150 offset:8896
	ds_read_b64_tr_b16 v[224:225], v150 offset:13248
	ds_read_b64_tr_b16 v[226:227], v150 offset:17600
	s_waitcnt lgkmcnt(13)
	v_mfma_f32_16x16x32_bf16 v[132:135], v[108:111], v[84:87], 0
	s_waitcnt lgkmcnt(11)
	v_mfma_f32_16x16x32_bf16 v[132:135], v[112:115], v[88:91], v[132:135]
	s_waitcnt lgkmcnt(9)
	v_mfma_f32_16x16x32_bf16 v[132:135], v[116:119], v[92:95], v[132:135]
	s_waitcnt lgkmcnt(7)
	v_mfma_f32_16x16x32_bf16 v[132:135], v[120:123], v[96:99], v[132:135]
	s_waitcnt lgkmcnt(5)
	v_mfma_f32_16x16x32_bf16 v[132:135], v[124:127], v[100:103], v[132:135]
	ds_read_b64_tr_b16 v[228:229], v150 offset:21952
	ds_read_b64_tr_b16 v[230:231], v150 offset:26304
	ds_read_b64_tr_b16 v[232:233], v150 offset:30656
	ds_read_b64_tr_b16 v[234:235], v150 offset:35008
	ds_read_b64_tr_b16 v[236:237], v150 offset:39360
	s_nop 2
	v_mul_f32_e32 v132, v250, v132
	v_mul_f32_e32 v133, v250, v133
	v_mul_f32_e32 v134, v250, v134
	v_mul_f32_e32 v135, v250, v135
	v_med3_f32 v132, v132, s41, v212
	v_med3_f32 v133, v133, s41, v212
	v_med3_f32 v134, v134, s41, v212
	v_med3_f32 v135, v135, s41, v212
	v_cvt_pk_fp8_f32 v251, v132, v133
	s_nop 0
	v_cvt_pk_fp8_f32 v251, v134, v135 op_sel:[0,0,1]
	s_nop 0
	global_store_dword v[104:105], v251, off offset:80
	ds_read_b64_tr_b16 v[108:109], v150 offset:224
	ds_read_b64_tr_b16 v[110:111], v150 offset:4576
	ds_read_b64_tr_b16 v[112:113], v150 offset:8928
	ds_read_b64_tr_b16 v[114:115], v150 offset:13280
	ds_read_b64_tr_b16 v[116:117], v150 offset:17632
	s_waitcnt lgkmcnt(13)
	v_mfma_f32_16x16x32_bf16 v[128:131], v[218:221], v[84:87], 0
	s_waitcnt lgkmcnt(11)
	v_mfma_f32_16x16x32_bf16 v[128:131], v[222:225], v[88:91], v[128:131]
	s_waitcnt lgkmcnt(9)
	v_mfma_f32_16x16x32_bf16 v[128:131], v[226:229], v[92:95], v[128:131]
	s_waitcnt lgkmcnt(7)
	v_mfma_f32_16x16x32_bf16 v[128:131], v[230:233], v[96:99], v[128:131]
	s_waitcnt lgkmcnt(5)
	v_mfma_f32_16x16x32_bf16 v[128:131], v[234:237], v[100:103], v[128:131]
	ds_read_b64_tr_b16 v[118:119], v150 offset:21984
	ds_read_b64_tr_b16 v[120:121], v150 offset:26336
	ds_read_b64_tr_b16 v[122:123], v150 offset:30688
	ds_read_b64_tr_b16 v[124:125], v150 offset:35040
	ds_read_b64_tr_b16 v[126:127], v150 offset:39392
	s_nop 2
	v_mul_f32_e32 v128, v250, v128
	v_mul_f32_e32 v129, v250, v129
	v_mul_f32_e32 v130, v250, v130
	v_mul_f32_e32 v131, v250, v131
	v_med3_f32 v128, v128, s41, v212
	v_med3_f32 v129, v129, s41, v212
	v_med3_f32 v130, v130, s41, v212
	v_med3_f32 v131, v131, s41, v212
	v_cvt_pk_fp8_f32 v251, v128, v129
	s_nop 0
	v_cvt_pk_fp8_f32 v251, v130, v131 op_sel:[0,0,1]
	s_nop 0
	global_store_dword v[104:105], v251, off offset:96
	s_waitcnt lgkmcnt(8)
	v_mfma_f32_16x16x32_bf16 v[132:135], v[108:111], v[84:87], 0
	s_waitcnt lgkmcnt(6)
	v_mfma_f32_16x16x32_bf16 v[132:135], v[112:115], v[88:91], v[132:135]
	s_waitcnt lgkmcnt(4)
	v_mfma_f32_16x16x32_bf16 v[132:135], v[116:119], v[92:95], v[132:135]
	s_waitcnt lgkmcnt(2)
	v_mfma_f32_16x16x32_bf16 v[132:135], v[120:123], v[96:99], v[132:135]
	s_waitcnt lgkmcnt(0)
	v_mfma_f32_16x16x32_bf16 v[132:135], v[124:127], v[100:103], v[132:135]
	s_nop 7
	v_mul_f32_e32 v132, v250, v132
	v_mul_f32_e32 v133, v250, v133
	v_mul_f32_e32 v134, v250, v134
	v_mul_f32_e32 v135, v250, v135
	v_med3_f32 v132, v132, s41, v212
	v_med3_f32 v133, v133, s41, v212
	v_med3_f32 v134, v134, s41, v212
	v_med3_f32 v135, v135, s41, v212
	v_cvt_pk_fp8_f32 v251, v132, v133
	s_nop 0
	v_cvt_pk_fp8_f32 v251, v134, v135 op_sel:[0,0,1]
	s_nop 0
	global_store_dword v[104:105], v251, off offset:112
	s_mov_b64 s[36:37], exec
	v_readlane_b32 s10, v254, 16
	v_readlane_b32 s11, v254, 17
	s_and_b64 s[10:11], s[36:37], s[10:11]
	s_mov_b64 exec, s[10:11]
	s_cbranch_execz .LBB0_706
	s_mov_b32 s10, 0x800000
	v_cmp_gt_f32_e32 vcc, s10, v106
	v_readlane_b32 s10, v254, 63
	v_mov_b32_e32 v85, v46
	v_cndmask_b32_e64 v84, 0, 32, vcc
	v_ldexp_f32 v84, v106, v84
	v_log_f32_e32 v86, v84
	v_lshl_or_b32 v84, v107, 3, s24
	v_readlane_b32 s11, v255, 0
	v_mul_f32_e32 v87, 0x3f317217, v86
	s_nop 0
	v_lshl_add_u64 v[84:85], v[84:85], 2, s[10:11]
	s_mov_b32 s10, 0x3f317217
	v_fma_f32 v87, v86, s10, -v87
	v_fmac_f32_e32 v87, 0x3377d1cf, v86
	s_mov_b32 s10, 0x7f800000
	v_fmac_f32_e32 v87, 0x3f317217, v86
	v_cmp_lt_f32_e64 s[10:11], |v86|, s10
	s_nop 1
	v_cndmask_b32_e64 v86, v86, v87, s[10:11]
	v_cndmask_b32_e32 v87, 0, v213, vcc
	v_sub_f32_e32 v86, v86, v87
	v_add_f32_e32 v47, v47, v86
	global_store_dword v[84:85], v47, off
	s_branch .LBB0_706

	.amdhsa_kernel _Z3fwd4Args
		.amdhsa_group_segment_fixed_size 0
		.amdhsa_private_segment_fixed_size 0
		.amdhsa_kernarg_size 456
		.amdhsa_user_sgpr_count 2
		.amdhsa_user_sgpr_dispatch_ptr 0
		.amdhsa_user_sgpr_queue_ptr 0
		.amdhsa_user_sgpr_kernarg_segment_ptr 1
		.amdhsa_user_sgpr_dispatch_id 0
		.amdhsa_user_sgpr_kernarg_preload_length 0
		.amdhsa_user_sgpr_kernarg_preload_offset 0
		.amdhsa_user_sgpr_private_segment_size 0
		.amdhsa_uses_dynamic_stack 0
		.amdhsa_enable_private_segment 0
		.amdhsa_system_sgpr_workgroup_id_x 1
		.amdhsa_system_sgpr_workgroup_id_y 0
		.amdhsa_system_sgpr_workgroup_id_z 0
		.amdhsa_system_sgpr_workgroup_info 0
		.amdhsa_system_vgpr_workitem_id 0
		.amdhsa_next_free_vgpr 256
		.amdhsa_next_free_sgpr 102
		.amdhsa_accum_offset 256
		.amdhsa_reserve_vcc 1
		.amdhsa_float_round_mode_32 0
		.amdhsa_float_round_mode_16_64 0
		.amdhsa_float_denorm_mode_32 3
		.amdhsa_float_denorm_mode_16_64 3
		.amdhsa_dx10_clamp 1
		.amdhsa_ieee_mode 1
		.amdhsa_fp16_overflow 0
		.amdhsa_tg_split 0
		.amdhsa_exception_fp_ieee_invalid_op 0
		.amdhsa_exception_fp_denorm_src 0
		.amdhsa_exception_fp_ieee_div_zero 0
		.amdhsa_exception_fp_ieee_overflow 0
		.amdhsa_exception_fp_ieee_underflow 0
		.amdhsa_exception_fp_ieee_inexact 0
		.amdhsa_exception_int_div_zero 0
	.end_amdhsa_kernel

amdhsa.kernels:
  - .agpr_count:     0
    .args:
      - .offset:         0
        .size:           200
        .value_kind:     by_value
      - .offset:         200
        .size:           4
        .value_kind:     hidden_block_count_x
      - .offset:         204
        .size:           4
        .value_kind:     hidden_block_count_y
      - .offset:         208
        .size:           4
        .value_kind:     hidden_block_count_z
      - .offset:         212
        .size:           2
        .value_kind:     hidden_group_size_x
      - .offset:         214
        .size:           2
        .value_kind:     hidden_group_size_y
      - .offset:         216
        .size:           2
        .value_kind:     hidden_group_size_z
      - .offset:         218
        .size:           2
        .value_kind:     hidden_remainder_x
      - .offset:         220
        .size:           2
        .value_kind:     hidden_remainder_y
      - .offset:         222
        .size:           2
        .value_kind:     hidden_remainder_z
      - .offset:         240
        .size:           8
        .value_kind:     hidden_global_offset_x
      - .offset:         248
        .size:           8
        .value_kind:     hidden_global_offset_y
      - .offset:         256
        .size:           8
        .value_kind:     hidden_global_offset_z
      - .offset:         264
        .size:           2
        .value_kind:     hidden_grid_dims
      - .offset:         320
        .size:           4
        .value_kind:     hidden_dynamic_lds_size
    .group_segment_fixed_size: 0
    .kernarg_segment_align: 8
    .kernarg_segment_size: 456
    .language:       OpenCL C
    .language_version:
      - 2
      - 0
    .max_flat_workgroup_size: 512
    .name:           _Z3fwd4Args
    .private_segment_fixed_size: 0
    .sgpr_count:     108
    .sgpr_spill_count: 87
    .symbol:         _Z3fwd4Args.kd
    .uniform_work_group_size: 1
    .uses_dynamic_stack: false
    .vgpr_count:     256
    .vgpr_spill_count: 0
    .wavefront_size: 64
